# v65 + in-proj tile order r0: gelu-stat,gelu-stat,rope,rope; r1: gelu,gelu,rope,rope (variant of v69 with the two gelu kinds swapped)
# speedup vs baseline: 1.0276x; 1.0212x over previous
;     __device__ bool next(int i, Unit& u) const { if (!base.next(i >> 1, u)) return false; if (i & 1) { u.pm += MTOK / BM; u.pn += DM / BM; } return true; }
;   __device__ __forceinline__ bool next(int i,AttnUnit&u)const{ if(i>=2||vcu>=256)return false; const int s=vcu&3; u.bh=vcu>>2; u.qb=(i==0)?7-s:s; return true; }
;     __host__ __device__ bool next(int i, Unit& u) const {
;         const int L = i * G + c; if (L >= nwg) return false;
;         int wgid = L; { const int q = nwg / NXCD, r = nwg % NXCD, xcd = wgid % NXCD, off = wgid / NXCD; wgid = (xcd < r ? xcd * (q + 1) : r * (q + 1) + (xcd - r) * q) + off; }
;         const int nig = WGM * nN, gid = wgid / nig, fm = gid * WGM, gsz = (nM - fm) < WGM ? (nM - fm) : WGM;
;         u.pm = fm + ((wgid % nig) % gsz); u.pn = (wgid % nig) / gsz; u.half = 0; return true;
.LBB0_382:
	s_ashr_i32 s4, s21, 31
	s_lshr_b32 s4, s4, 29
	s_add_i32 s4, s21, s4
	s_ashr_i32 s5, s4, 3
	s_and_b32 s4, s4, -8
	s_sub_i32 s4, s21, s4
	s_cmp_lt_i32 s4, 0
	s_movk_i32 s6, 0x91
	s_cselect_b32 s6, s6, 0x90
	s_mul_i32 s4, s4, s6
	s_add_i32 s4, s4, s5
	s_mul_hi_i32 s5, s4, 0x38e38e39
	s_lshr_b32 s6, s5, 31
	s_ashr_i32 s5, s5, 5
	s_add_i32 s5, s5, s6
	s_lshl_b32 s6, s5, 3
	s_mulk_i32 s5, 0x90
	s_sub_i32 s4, s4, s5
	s_bfe_u32 s5, s4, 0x3001c
	s_add_i32 s5, s4, s5
	s_sext_i32_i16 s7, s5
	s_and_b32 s5, s5, 0xfff8
	s_sub_i32 s4, s4, s5
	s_sext_i32_i16 s4, s4
	s_add_i32 s18, s6, s4
	s_ashr_i32 s70, s7, 3
	s_mul_i32 s4, s70, 5
	s_cmp_lt_u32 s70, 12
	s_cbranch_scc0 .Lpn_hi0
	s_mov_b32 s6, 0x82029062
	s_mov_b32 s7, 0x5a92839
	s_branch .Lpn_go0

;     __device__ bool next(int i, Unit& u) const { if (!base.next(i >> 1, u)) return false; if (i & 1) { u.pm += MTOK / BM; u.pn += DM / BM; } return true; }
;   __device__ __forceinline__ bool next(int i,AttnUnit&u)const{ if(i>=2||vcu>=256)return false; const int s=vcu&3; u.bh=vcu>>2; u.qb=(i==0)?7-s:s; return true; }
;     __host__ __device__ bool next(int i, Unit& u) const {
;         const int L = i * G + c; if (L >= nwg) return false;
;         int wgid = L; { const int q = nwg / NXCD, r = nwg % NXCD, xcd = wgid % NXCD, off = wgid / NXCD; wgid = (xcd < r ? xcd * (q + 1) : r * (q + 1) + (xcd - r) * q) + off; }
;         const int nig = WGM * nN, gid = wgid / nig, fm = gid * WGM, gsz = (nM - fm) < WGM ? (nM - fm) : WGM;
;         u.pm = fm + ((wgid % nig) % gsz); u.pn = (wgid % nig) / gsz; u.half = 0; return true;
; template <class Epi, class Sched, bool ALIGN_EPI = false, bool SP2 = false>
; __device__ __forceinline__ void gemm_phase(PG8_LAS unsigned char* lds, const Gemm g, const Sched& S, const Epi& E) {
;     ...
;         const bool has_next = S.next(ui + 1, nxt);
;         const char* nA = has_next ? (const char*)g.A + (size_t)nxt.pm * tstep + (nxt.half == 2 ? hstep : (size_t)0) : cA; const char* nB = has_next ? (const char*)g.Bt + (size_t)nxt.pn * tstep : cB;
.LBB0_392:
	s_add_i32 s72, s72, 1
	s_mul_i32 s10, s72, s33
	s_add_i32 s10, s10, s21
	s_cmpk_lt_i32 s10, 0x480
	s_cselect_b64 s[64:65], -1, 0
	s_cmpk_gt_i32 s10, 0x47f
	s_cbranch_scc1 .LBB0_394
	s_ashr_i32 s11, s10, 31
	s_lshr_b32 s11, s11, 29
	s_add_i32 s11, s10, s11
	s_ashr_i32 s12, s11, 3
	s_and_b32 s11, s11, -8
	s_sub_i32 s10, s10, s11
	s_cmp_lt_i32 s10, 0
	s_movk_i32 s11, 0x91
	s_cselect_b32 s11, s11, 0x90
	s_mul_i32 s10, s10, s11
	s_add_i32 s10, s10, s12
	s_mul_hi_i32 s11, s10, 0x38e38e39
	s_lshr_b32 s12, s11, 31
	s_ashr_i32 s11, s11, 5
	s_add_i32 s11, s11, s12
	s_lshl_b32 s12, s11, 3
	s_mulk_i32 s11, 0x90
	s_sub_i32 s10, s10, s11
	s_bfe_u32 s11, s10, 0x3001c
	s_add_i32 s11, s10, s11
	s_sext_i32_i16 s13, s11
	s_and_b32 s11, s11, 0xfff8
	s_sub_i32 s10, s10, s11
	s_sext_i32_i16 s10, s10
	s_add_i32 s60, s12, s10
	s_ashr_i32 s62, s13, 3
	s_mul_i32 s10, s62, 5
	s_cmp_lt_u32 s62, 12
	s_cbranch_scc0 .Lpn_hi1
	s_mov_b32 s12, 0x82029062
	s_mov_b32 s13, 0x5a92839
	s_branch .Lpn_go1
